# v38 + next-layer SSM-matrix prep split four ways across workgroups (each builds the LDS intermediates, writes a quarter of the outputs)
# baseline (speedup 1.0000x reference)
.LBB0_1411:
	s_cmp_eq_u32 s76, 3
	s_cbranch_scc1 .LBB0_1587
	v_readlane_b32 s0, v254, 47
	v_readlane_b32 s2, v253, 27
	v_readlane_b32 s3, v253, 28
	v_mov_b32_e32 v1, s0
	ds_read_b32 v1, v1
	s_waitcnt lgkmcnt(0)
	s_barrier
	v_readfirstlane_b32 s0, v1
	s_lshl_b32 s0, s0, 2
	s_ashr_i32 s1, s0, 31
	s_abs_i32 s0, s0
	s_mul_hi_u32 s2, s0, s2
	s_mul_i32 s2, s2, s3
	s_sub_i32 s0, s0, s2
	s_sub_i32 s2, s0, s3
	s_cmp_ge_u32 s0, s3
	s_cselect_b32 s0, s2, s0
	s_sub_i32 s2, s0, s3
	s_cmp_ge_u32 s0, s3
	s_cselect_b32 s0, s2, s0
	s_xor_b32 s0, s0, s1
	s_sub_i32 s0, s0, s1
	s_cmp_lt_i32 s88, s0
	s_cbranch_scc1 .LBB0_1587
	s_sub_i32 s45, s88, s0
	s_sub_i32 s33, s78, s0
	v_readlane_b32 s0, v253, 61
	v_mov_b32_e32 v22, v232
	v_readlane_b32 s4, v253, 63
	v_mov_b32_e32 v2, s0
	ds_read_b64 v[4:5], v2
	v_readlane_b32 s0, v253, 62
	v_readlane_b32 s8, v254, 0
	v_readlane_b32 s12, v254, 1
	v_mov_b32_e32 v2, s0
	s_waitcnt lgkmcnt(0)
	v_readfirstlane_b32 s21, v5
	v_readfirstlane_b32 s20, v4
	ds_read_b128 v[4:7], v2
	v_mov_b32_e32 v2, s4
	s_add_i32 s92, s76, 1
	v_ashrrev_i32_e32 v1, 6, v22
	v_and_b32_e32 v23, 63, v22
	s_waitcnt lgkmcnt(0)
	v_readfirstlane_b32 s1, v5
	v_readfirstlane_b32 s3, v4
	v_readfirstlane_b32 s0, v7
	v_readfirstlane_b32 s2, v6
	ds_read_b128 v[4:7], v2
	v_mov_b32_e32 v2, s8
	v_readfirstlane_b32 s44, v1
	s_cmp_gt_i32 s33, 127
	s_cselect_b32 s14, 127, 31
	s_cmp_gt_i32 s45, s14
	s_waitcnt lgkmcnt(0)
	v_readfirstlane_b32 s5, v5
	v_readfirstlane_b32 s7, v4
	v_readfirstlane_b32 s4, v7
	v_readfirstlane_b32 s6, v6
	ds_read_b128 v[4:7], v2
	v_mov_b32_e32 v2, s12
	s_waitcnt lgkmcnt(0)
	v_readfirstlane_b32 s9, v5
	v_readfirstlane_b32 s11, v4
	ds_read_b64 v[4:5], v2
	v_readfirstlane_b32 s8, v7
	v_readfirstlane_b32 s10, v6
	s_waitcnt lgkmcnt(0)
	v_readfirstlane_b32 s12, v5
	v_readfirstlane_b32 s13, v4
	s_cbranch_scc1 .LBB0_1459
	s_lshl_b64 s[14:15], s[92:93], 13
	s_add_u32 s18, s3, s14
	s_addc_u32 s19, s1, s15
	s_add_u32 s22, s2, s14
	s_addc_u32 s23, s0, s15
	s_lshl_b32 s0, s92, 5
	s_mov_b32 s1, s93
	s_lshl_b64 s[0:1], s[0:1], 2
	s_add_u32 s46, s7, s0
	s_addc_u32 s47, s5, s1
	s_lshl_b64 s[0:1], s[92:93], 17
	s_add_u32 s24, s6, s0
	s_addc_u32 s25, s4, s1
	s_add_u32 s26, s11, s0
	s_addc_u32 s27, s9, s1
	s_add_u32 s28, s10, s0
	s_addc_u32 s29, s8, s1
	s_add_u32 s30, s13, s0
	s_addc_u32 s31, s12, s1
	s_movk_i32 s0, 0x440
	v_cmp_gt_i32_e64 s[2:3], s0, v22
	s_movk_i32 s0, 0x400
	s_add_u32 s48, s20, 0x27e0000
	v_cmp_gt_i32_e64 s[4:5], s0, v22
	s_movk_i32 s0, 0x1000
	s_addc_u32 s49, s21, 0
	v_cmp_gt_i32_e64 s[6:7], s0, v22
	s_add_u32 s50, s20, 0x23e0000
	s_mov_b32 s0, 0xc000
	s_addc_u32 s51, s21, 0
	v_cmp_gt_i32_e64 s[8:9], s0, v22
	s_mov_b32 s0, 0x8000
	v_cmp_gt_i32_e64 s[10:11], s0, v22
	s_add_u32 s34, s20, 0x1100000
	v_lshlrev_b32_e32 v2, 3, v22
	v_and_b32_e32 v4, 15, v22
	v_readlane_b32 s0, v254, 2
	v_cmp_gt_i32_e64 s[12:13], 64, v22
	s_addc_u32 s35, s21, 0
	v_add_u32_e32 v12, 0, v2
	v_add_u32_e32 v13, s0, v2
	s_lshl_b32 s52, s45, 10
	s_lshl_b32 s53, s33, 10
	v_lshlrev_b32_e32 v14, 2, v22
	v_lshl_add_u32 v15, v4, 3, s0
	v_lshlrev_b32_e32 v16, 1, v22
	s_cmp_gt_i32 s33, 127
	s_cbranch_scc1 .Lssm_split
	s_mov_b32 s36, s45
	v_mov_b32_e32 v135, 0xbdff
	v_mov_b32_e32 v136, 0x7dff
	v_mov_b32_e32 v137, 0
	v_mov_b32_e32 v138, 0
	v_mov_b32_e32 v139, 0
	v_mov_b32_e32 v140, 0
	s_branch .LBB0_1416
.Lssm_split:
	s_lshr_b32 s0, s45, 5
	s_and_b32 s36, s45, 31
	s_lshl_b32 s52, s36, 10
	s_mul_i32 s1, s0, 0x3000
	v_mov_b32_e32 v138, s1
	s_lshl_b32 s1, s1, 1
	v_mov_b32_e32 v137, s1
	v_add_u32_e32 v135, 0x2dff, v138
	s_lshl_b32 s1, s0, 13
	v_mov_b32_e32 v140, s1
	s_lshl_b32 s1, s1, 1
	v_mov_b32_e32 v139, s1
	v_add_u32_e32 v136, 0x1dff, v140
	s_branch .LBB0_1416

.LBB0_1435:
	s_or_b64 exec, exec, s[0:1]
	s_waitcnt lgkmcnt(0)
	s_barrier
	s_and_saveexec_b64 s[14:15], s[8:9]
	s_cbranch_execz .LBB0_1450
	s_mul_i32 s1, s36, 0x30000
	s_mul_hi_i32 s0, s36, 0x30000
	s_add_u32 s16, s48, s1
	s_addc_u32 s17, s49, s0
	s_mov_b64 s[38:39], 0
	v_add_u32_e32 v2, v137, v16
	v_add_u32_e32 v6, v138, v22
	s_branch .LBB0_1439

.LBB0_1438:
	s_or_b64 exec, exec, s[0:1]
	s_waitcnt lgkmcnt(0)
	v_bfe_u32 v8, v7, 16, 1
	v_add3_u32 v7, v7, v8, s86
	v_bfe_u32 v8, v11, 16, 1
	v_lshrrev_b32_e32 v7, 16, v7
	v_add3_u32 v8, v11, v8, s86
	v_and_or_b32 v7, v8, s87, v7
	v_mov_b64_e32 v[8:9], s[16:17]
	s_movk_i32 s0, 0x300
	v_mad_i64_i32 v[8:9], s[0:1], v5, s0, v[8:9]
	v_ashrrev_i32_e32 v5, 31, v4
	v_lshl_add_u64 v[4:5], v[4:5], 1, v[8:9]
	s_mov_b32 s0, 0xbdff
	global_store_dword v[4:5], v7, off
	v_add_u32_e32 v4, 0x200, v6
	v_cmp_lt_i32_e32 vcc, v135, v6
	v_add_u32_e32 v2, 0x400, v2
	s_or_b64 s[38:39], vcc, s[38:39]
	v_mov_b32_e32 v6, v4
	s_andn2_b64 exec, exec, s[38:39]
	s_cbranch_execz .LBB0_1450

.LBB0_1450:
	s_or_b64 exec, exec, s[14:15]
	s_and_saveexec_b64 s[14:15], s[10:11]
	s_cbranch_execz .LBB0_1457
	s_lshl_b64 s[0:1], s[36:37], 17
	s_add_u32 s16, s50, s0
	s_addc_u32 s17, s51, s1
	s_mov_b64 s[38:39], 0
	v_add_u32_e32 v6, v139, v16
	v_add_u32_e32 v7, v140, v22
	s_branch .LBB0_1453
.LBB0_1452:
	s_or_b64 exec, exec, s[40:41]
	v_bfe_u32 v5, v10, 16, 1
	v_add3_u32 v5, v10, v5, s86
	v_bfe_u32 v9, v2, 16, 1
	v_lshrrev_b32_e32 v5, 16, v5
	v_add3_u32 v2, v2, v9, s86
	v_and_or_b32 v9, v2, s87, v5
	v_ashrrev_i32_e32 v5, 31, v4
	v_and_b32_e32 v8, 0xfe, v6
	v_lshlrev_b64 v[4:5], 9, v[4:5]
	v_lshl_add_u64 v[4:5], s[16:17], 0, v[4:5]
	v_lshlrev_b32_e32 v2, 1, v8
	s_movk_i32 s0, 0x7dff
	v_lshl_add_u64 v[4:5], v[4:5], 0, v[2:3]
	v_add_u32_e32 v2, 0x200, v7
	v_cmp_lt_i32_e32 vcc, v136, v7
	v_add_u32_e32 v6, 0x400, v6
	s_or_b64 s[38:39], vcc, s[38:39]
	v_mov_b32_e32 v7, v2
	global_store_dword v[4:5], v9, off
	s_andn2_b64 exec, exec, s[38:39]
	s_cbranch_execz .LBB0_1457
